# norm phases: __shfl_xor butterflies (ds_bpermute + wait per step) replaced by DPP quad_perm/row_mirror + permlane16/32 swaps, same pairing order
# speedup vs baseline: 1.0062x; 1.0062x over previous
.LBB0_229:
	v_lshl_add_u64 v[100:101], v[46:47], 0, s[20:21]
	global_load_dwordx4 v[84:87], v[100:101], off
	global_load_dwordx4 v[88:91], v[100:101], off offset:1024
	global_load_dwordx4 v[92:95], v[100:101], off offset:2048
	global_load_dwordx4 v[96:99], v[100:101], off offset:3072
	v_add_co_u32_e32 v112, vcc, s7, v100
	s_waitcnt vmcnt(3)
	v_mov_b32_e32 v134, v85
	v_addc_co_u32_e32 v113, vcc, 0, v101, vcc
	global_load_dwordx4 v[100:103], v[112:113], off
	global_load_dwordx4 v[104:107], v[112:113], off offset:1024
	global_load_dwordx4 v[108:111], v[112:113], off offset:3072
	s_nop 0
	global_load_dwordx4 v[112:115], v[112:113], off offset:2048
	s_waitcnt vmcnt(6)
	v_mov_b32_e32 v135, v89
	v_mov_b32_e32 v138, v87
	v_mov_b32_e32 v139, v91
	v_mov_b32_e32 v132, v84
	v_mov_b32_e32 v133, v88
	v_mov_b32_e32 v136, v86
	v_mov_b32_e32 v137, v90
	s_waitcnt vmcnt(5)
	v_pk_mul_f32 v[140:141], v[94:95], v[94:95]
	v_pk_mul_f32 v[142:143], v[92:93], v[92:93]
	v_pk_mul_f32 v[134:135], v[134:135], v[134:135]
	v_pk_mul_f32 v[138:139], v[138:139], v[138:139]
	v_pk_mov_b32 v[148:149], v[142:143], v[140:141] op_sel:[1,0]
	v_mov_b32_e32 v143, v141
	v_pk_fma_f32 v[132:133], v[132:133], v[132:133], v[134:135]
	v_pk_fma_f32 v[134:135], v[136:137], v[136:137], v[138:139]
	s_waitcnt vmcnt(4)
	v_mul_f32_e32 v144, v97, v97
	v_mul_f32_e32 v146, v99, v99
	v_pk_add_f32 v[136:137], v[148:149], v[142:143]
	v_pk_add_f32 v[132:133], v[132:133], v[134:135]
	v_pk_fma_f32 v[144:145], v[96:97], v[96:97], v[144:145] op_sel_hi:[1,1,0]
	v_pk_fma_f32 v[146:147], v[98:99], v[98:99], v[146:147] op_sel_hi:[1,1,0]
	v_pk_add_f32 v[136:137], v[136:137], v[136:137] op_sel:[0,1] op_sel_hi:[1,0]
	v_pk_add_f32 v[132:133], v[132:133], v[132:133] op_sel:[0,1] op_sel_hi:[1,0]
	s_waitcnt vmcnt(3)
	v_mul_f32_e32 v131, v100, v100
	v_mul_f32_e32 v153, v101, v101
	v_mul_f32_e32 v155, v102, v102
	v_mul_f32_e32 v156, v103, v103
	s_waitcnt vmcnt(2)
	v_pk_mul_f32 v[140:141], v[106:107], v[106:107]
	v_pk_mul_f32 v[150:151], v[104:105], v[104:105]
	v_mov_b32_e32 v145, v155
	v_mov_b32_e32 v147, v156
	v_mov_b32_e32 v137, v153
	v_mov_b32_e32 v133, v131
	v_pk_mov_b32 v[138:139], v[150:151], v[140:141] op_sel:[1,0]
	v_mov_b32_e32 v151, v141
	v_pk_add_f32 v[134:135], v[144:145], v[146:147]
	v_pk_add_f32 v[132:133], v[132:133], v[136:137]
	s_waitcnt vmcnt(0)
	v_mul_f32_e32 v152, v113, v113
	v_mul_f32_e32 v154, v115, v115
	v_pk_add_f32 v[138:139], v[138:139], v[150:151]
	v_pk_add_f32 v[132:133], v[132:133], v[134:135]
	v_mul_f32_e32 v157, v108, v108
	v_mul_f32_e32 v158, v109, v109
	v_mul_f32_e32 v159, v110, v110
	v_mul_f32_e32 v160, v111, v111
	v_pk_fma_f32 v[140:141], v[112:113], v[112:113], v[152:153] op_sel_hi:[1,1,0]
	v_pk_fma_f32 v[142:143], v[114:115], v[114:115], v[154:155] op_sel_hi:[1,1,0]
	v_pk_add_f32 v[138:139], v[138:139], v[138:139] op_sel:[0,1] op_sel_hi:[1,0]
	v_pk_add_f32 v[132:133], v[132:133], v[132:133] op_sel:[0,1] op_sel_hi:[1,0]
	v_mov_b32_e32 v141, v159
	v_mov_b32_e32 v143, v160
	v_mov_b32_e32 v139, v158
	v_mov_b32_e32 v133, v157
	v_pk_add_f32 v[140:141], v[140:141], v[142:143]
	v_pk_add_f32 v[132:133], v[132:133], v[138:139]
	s_nop 0
	v_pk_add_f32 v[132:133], v[132:133], v[140:141]
	s_nop 0
	v_add_f32_e32 v131, v132, v133
	s_nop 1
	v_add_f32_dpp v131, v131, v131 quad_perm:[1,0,3,2] row_mask:0xf bank_mask:0xf
	s_nop 1
	v_add_f32_dpp v131, v131, v131 quad_perm:[2,3,0,1] row_mask:0xf bank_mask:0xf
	s_nop 1
	v_add_f32_dpp v131, v131, v131 row_half_mirror row_mask:0xf bank_mask:0xf
	s_nop 1
	v_add_f32_dpp v131, v131, v131 row_mirror row_mask:0xf bank_mask:0xf
	v_mov_b32_e32 v132, v131
	s_nop 1
	v_permlane16_swap_b32_e32 v132, v131
	v_add_f32_e32 v131, v131, v132
	v_mov_b32_e32 v132, v131
	s_nop 1
	v_permlane32_swap_b32_e32 v132, v131
	v_add_f32_e32 v131, v131, v132
	v_fmamk_f32 v131, v131, 0x3a000000, v128
	v_mul_f32_e32 v132, 0x4f800000, v131
	v_cmp_gt_f32_e32 vcc, s9, v131
	s_nop 1
	v_cndmask_b32_e32 v131, v131, v132, vcc
	v_sqrt_f32_e32 v132, v131
	s_nop 0
	v_add_u32_e32 v133, -1, v132
	v_add_u32_e32 v134, 1, v132
	v_fma_f32 v135, -v133, v132, v131
	v_fma_f32 v136, -v134, v132, v131
	v_cmp_ge_f32_e64 s[4:5], 0, v135
	s_nop 1
	v_cndmask_b32_e64 v132, v132, v133, s[4:5]
	v_cmp_lt_f32_e64 s[4:5], 0, v136
	s_nop 1
	v_cndmask_b32_e64 v132, v132, v134, s[4:5]
	v_mul_f32_e32 v133, 0x37800000, v132
	v_cndmask_b32_e32 v132, v132, v133, vcc
	v_cmp_class_f32_e32 vcc, v131, v129
	s_nop 1
	v_cndmask_b32_e32 v131, v132, v131, vcc
	v_div_scale_f32 v132, s[4:5], v131, v131, 1.0
	v_rcp_f32_e32 v133, v132
	v_div_scale_f32 v134, vcc, 1.0, v131, 1.0
	v_fma_f32 v135, -v132, v133, 1.0
	v_fmac_f32_e32 v133, v135, v133
	v_mul_f32_e32 v135, v134, v133
	v_fma_f32 v136, -v132, v135, v134
	v_fmac_f32_e32 v135, v136, v133
	v_fma_f32 v132, -v132, v135, v134
	v_div_fmas_f32 v132, v132, v133, v135
	v_div_fixup_f32 v132, v132, v131, 1.0
	v_pk_mul_f32 v[86:87], v[86:87], v[132:133] op_sel_hi:[1,0]
	v_pk_mul_f32 v[90:91], v[90:91], v[132:133] op_sel_hi:[1,0]
	v_pk_mul_f32 v[84:85], v[84:85], v[132:133] op_sel_hi:[1,0]
	v_pk_mul_f32 v[88:89], v[88:89], v[132:133] op_sel_hi:[1,0]
	v_pk_mul_f32 v[92:93], v[92:93], v[132:133] op_sel_hi:[1,0]
	v_pk_mul_f32 v[94:95], v[94:95], v[132:133] op_sel_hi:[1,0]
	v_pk_mul_f32 v[96:97], v[96:97], v[132:133] op_sel_hi:[1,0]
	v_pk_mul_f32 v[98:99], v[98:99], v[132:133] op_sel_hi:[1,0]
	v_pk_mul_f32 v[134:135], v[100:101], v[132:133] op_sel_hi:[1,0]
	v_pk_mul_f32 v[136:137], v[102:103], v[132:133] op_sel_hi:[1,0]
	v_pk_mul_f32 v[138:139], v[104:105], v[132:133] op_sel_hi:[1,0]
	v_pk_mul_f32 v[140:141], v[106:107], v[132:133] op_sel_hi:[1,0]
	v_pk_mul_f32 v[142:143], v[112:113], v[132:133] op_sel_hi:[1,0]
	v_pk_mul_f32 v[144:145], v[114:115], v[132:133] op_sel_hi:[1,0]
	v_pk_mul_f32 v[146:147], v[108:109], v[132:133] op_sel_hi:[1,0]
	v_pk_mul_f32 v[132:133], v[110:111], v[132:133] op_sel_hi:[1,0]
	v_pk_fma_f32 v[112:113], v[50:51], v[86:87], v[4:5]
	v_pk_fma_f32 v[108:109], v[54:55], v[90:91], v[8:9]
	v_pk_fma_f32 v[114:115], v[52:53], v[84:85], v[2:3]
	v_pk_fma_f32 v[110:111], v[56:57], v[88:89], v[6:7]
	v_pk_fma_f32 v[104:105], v[58:59], v[94:95], v[12:13]
	v_pk_fma_f32 v[100:101], v[62:63], v[98:99], v[16:17]
	v_pk_fma_f32 v[84:85], v[78:79], v[132:133], v[32:33]
	v_max_f32_e64 v131, |v112|, |v113|
	v_max_f32_e64 v132, |v108|, |v109|
	v_pk_fma_f32 v[106:107], v[60:61], v[92:93], v[10:11]
	v_pk_fma_f32 v[102:103], v[64:65], v[96:97], v[14:15]
	v_pk_fma_f32 v[96:97], v[66:67], v[136:137], v[20:21]
	v_pk_fma_f32 v[98:99], v[68:69], v[134:135], v[18:19]
	v_pk_fma_f32 v[92:93], v[70:71], v[140:141], v[24:25]
	v_max_f32_e64 v133, |v104|, |v105|
	v_max_f32_e64 v134, |v100|, |v101|
	v_max3_f32 v131, |v114|, |v115|, v131
	v_max3_f32 v132, |v110|, |v111|, v132
	v_pk_fma_f32 v[94:95], v[72:73], v[138:139], v[22:23]
	v_pk_fma_f32 v[88:89], v[74:75], v[144:145], v[28:29]
	v_max_f32_e64 v135, |v96|, |v97|
	v_max_f32_e64 v136, |v92|, |v93|
	v_max3_f32 v133, |v106|, |v107|, v133
	v_max3_f32 v134, |v102|, |v103|, v134
	v_max3_f32 v131, v131, s24, v132
	v_pk_fma_f32 v[90:91], v[76:77], v[142:143], v[26:27]
	v_pk_fma_f32 v[86:87], v[80:81], v[146:147], v[30:31]
	v_max_f32_e64 v137, |v88|, |v89|
	v_max_f32_e64 v138, |v84|, |v85|
	v_max3_f32 v135, |v98|, |v99|, v135
	v_max3_f32 v136, |v94|, |v95|, v136
	v_max3_f32 v131, v131, v133, v134
	v_max3_f32 v137, |v90|, |v91|, v137
	v_max3_f32 v131, v131, v135, v136
	v_max3_f32 v132, |v86|, |v87|, v138
	v_max3_f32 v131, v131, v137, v132
	s_nop 1
	v_max_f32_dpp v131, v131, v131 quad_perm:[1,0,3,2] row_mask:0xf bank_mask:0xf
	s_nop 1
	v_max_f32_dpp v131, v131, v131 quad_perm:[2,3,0,1] row_mask:0xf bank_mask:0xf
	s_nop 1
	v_max_f32_dpp v131, v131, v131 row_half_mirror row_mask:0xf bank_mask:0xf
	s_nop 1
	v_max_f32_dpp v131, v131, v131 row_mirror row_mask:0xf bank_mask:0xf
	v_mov_b32_e32 v132, v131
	s_nop 1
	v_permlane16_swap_b32_e32 v132, v131
	v_max_f32_e32 v131, v131, v132
	v_mov_b32_e32 v132, v131
	s_nop 1
	v_permlane32_swap_b32_e32 v132, v131
	v_max_f32_e32 v131, v131, v132
	s_and_saveexec_b64 s[4:5], s[0:1]
	s_cbranch_execz .LBB0_228
	v_mul_f32_e32 v132, 0x3c010204, v131
	global_store_dword v35, v132, s[22:23]
	s_branch .LBB0_228

.LBB0_1122:
	global_load_dwordx2 v[86:87], v[50:51], off offset:-2048
	global_load_dwordx2 v[88:89], v[50:51], off offset:-1536
	global_load_dwordx2 v[90:91], v[50:51], off offset:-1024
	global_load_dwordx2 v[92:93], v[50:51], off offset:-512
	global_load_dwordx2 v[94:95], v[50:51], off
	global_load_dwordx2 v[96:97], v[50:51], off offset:512
	global_load_dwordx2 v[98:99], v[50:51], off offset:1024
	global_load_dwordx2 v[100:101], v[50:51], off offset:1536
	s_waitcnt vmcnt(7)
	v_cvt_f32_f16_sdwa v103, v86 dst_sel:DWORD dst_unused:UNUSED_PAD src0_sel:WORD_1
	v_cvt_f32_f16_sdwa v105, v87 dst_sel:DWORD dst_unused:UNUSED_PAD src0_sel:WORD_1
	v_cvt_f32_f16_e32 v104, v87
	s_waitcnt vmcnt(6)
	v_cvt_f32_f16_sdwa v87, v88 dst_sel:DWORD dst_unused:UNUSED_PAD src0_sel:WORD_1
	v_cvt_f32_f16_sdwa v107, v89 dst_sel:DWORD dst_unused:UNUSED_PAD src0_sel:WORD_1
	v_cvt_f32_f16_e32 v102, v86
	v_cvt_f32_f16_e32 v86, v88
	v_cvt_f32_f16_e32 v106, v89
	s_waitcnt vmcnt(5)
	v_cvt_f32_f16_sdwa v89, v90 dst_sel:DWORD dst_unused:UNUSED_PAD src0_sel:WORD_1
	v_cvt_f32_f16_sdwa v109, v91 dst_sel:DWORD dst_unused:UNUSED_PAD src0_sel:WORD_1
	v_cvt_f32_f16_e32 v88, v90
	v_cvt_f32_f16_e32 v108, v91
	s_waitcnt vmcnt(4)
	v_cvt_f32_f16_sdwa v91, v92 dst_sel:DWORD dst_unused:UNUSED_PAD src0_sel:WORD_1
	v_cvt_f32_f16_sdwa v111, v93 dst_sel:DWORD dst_unused:UNUSED_PAD src0_sel:WORD_1
	v_cvt_f32_f16_e32 v90, v92
	v_cvt_f32_f16_e32 v110, v93
	s_waitcnt vmcnt(3)
	v_cvt_f32_f16_sdwa v93, v94 dst_sel:DWORD dst_unused:UNUSED_PAD src0_sel:WORD_1
	v_cvt_f32_f16_e32 v92, v94
	v_cvt_f32_f16_sdwa v113, v95 dst_sel:DWORD dst_unused:UNUSED_PAD src0_sel:WORD_1
	v_cvt_f32_f16_e32 v112, v95
	s_waitcnt vmcnt(1)
	v_cvt_f32_f16_sdwa v135, v98 dst_sel:DWORD dst_unused:UNUSED_PAD src0_sel:WORD_1
	v_cvt_f32_f16_e32 v134, v98
	v_cvt_f32_f16_sdwa v137, v99 dst_sel:DWORD dst_unused:UNUSED_PAD src0_sel:WORD_1
	v_cvt_f32_f16_e32 v136, v99
	v_mov_b32_e32 v98, v103
	v_mov_b32_e32 v99, v87
	v_mov_b32_e32 v116, v105
	v_mov_b32_e32 v117, v107
	v_cvt_f32_f16_sdwa v95, v96 dst_sel:DWORD dst_unused:UNUSED_PAD src0_sel:WORD_1
	v_cvt_f32_f16_e32 v94, v96
	v_cvt_f32_f16_sdwa v115, v97 dst_sel:DWORD dst_unused:UNUSED_PAD src0_sel:WORD_1
	v_cvt_f32_f16_e32 v114, v97
	s_waitcnt vmcnt(0)
	v_cvt_f32_f16_sdwa v139, v100 dst_sel:DWORD dst_unused:UNUSED_PAD src0_sel:WORD_1
	v_cvt_f32_f16_e32 v138, v100
	v_cvt_f32_f16_sdwa v141, v101 dst_sel:DWORD dst_unused:UNUSED_PAD src0_sel:WORD_1
	v_cvt_f32_f16_e32 v140, v101
	v_mov_b32_e32 v96, v102
	v_mov_b32_e32 v97, v86
	v_mov_b32_e32 v100, v104
	v_mov_b32_e32 v101, v106
	v_mov_b32_e32 v144, v89
	v_mov_b32_e32 v145, v109
	v_pk_mul_f32 v[98:99], v[98:99], v[98:99]
	v_pk_mul_f32 v[116:117], v[116:117], v[116:117]
	v_mov_b32_e32 v142, v88
	v_mov_b32_e32 v143, v108
	v_pk_mul_f32 v[144:145], v[144:145], v[144:145]
	v_pk_fma_f32 v[96:97], v[96:97], v[96:97], v[98:99]
	v_pk_fma_f32 v[98:99], v[100:101], v[100:101], v[116:117]
	v_mul_f32_e32 v146, v91, v91
	v_mul_f32_e32 v148, v111, v111
	v_pk_fma_f32 v[100:101], v[142:143], v[142:143], v[144:145]
	v_pk_add_f32 v[96:97], v[96:97], v[98:99]
	v_pk_mul_f32 v[150:151], v[92:93], v[92:93]
	v_pk_mul_f32 v[152:153], v[112:113], v[112:113]
	v_pk_fma_f32 v[146:147], v[90:91], v[90:91], v[146:147] op_sel_hi:[1,1,0]
	v_pk_fma_f32 v[148:149], v[110:111], v[110:111], v[148:149] op_sel_hi:[1,1,0]
	v_pk_add_f32 v[98:99], v[100:101], v[100:101] op_sel:[0,1] op_sel_hi:[1,0]
	v_pk_add_f32 v[96:97], v[96:97], v[96:97] op_sel:[0,1] op_sel_hi:[1,0]
	v_mov_b32_e32 v156, v95
	v_mov_b32_e32 v157, v115
	v_mov_b32_e32 v147, v152
	v_mov_b32_e32 v149, v153
	v_mov_b32_e32 v99, v151
	v_mov_b32_e32 v97, v150
	v_mov_b32_e32 v154, v94
	v_mov_b32_e32 v155, v114
	v_pk_mul_f32 v[156:157], v[156:157], v[156:157]
	v_pk_add_f32 v[100:101], v[146:147], v[148:149]
	v_pk_add_f32 v[96:97], v[96:97], v[98:99]
	v_mul_f32_e32 v158, v135, v135
	v_mul_f32_e32 v160, v137, v137
	v_pk_fma_f32 v[116:117], v[154:155], v[154:155], v[156:157]
	v_pk_add_f32 v[96:97], v[96:97], v[100:101]
	v_pk_mul_f32 v[162:163], v[138:139], v[138:139]
	v_pk_mul_f32 v[164:165], v[140:141], v[140:141]
	v_pk_fma_f32 v[158:159], v[134:135], v[134:135], v[158:159] op_sel_hi:[1,1,0]
	v_pk_fma_f32 v[160:161], v[136:137], v[136:137], v[160:161] op_sel_hi:[1,1,0]
	v_pk_add_f32 v[116:117], v[116:117], v[116:117] op_sel:[0,1] op_sel_hi:[1,0]
	v_pk_add_f32 v[96:97], v[96:97], v[96:97] op_sel:[0,1] op_sel_hi:[1,0]
	v_mov_b32_e32 v159, v164
	v_mov_b32_e32 v161, v165
	v_mov_b32_e32 v117, v163
	v_mov_b32_e32 v97, v162
	v_pk_add_f32 v[142:143], v[158:159], v[160:161]
	v_pk_add_f32 v[96:97], v[96:97], v[116:117]
	s_nop 0
	v_pk_add_f32 v[96:97], v[96:97], v[142:143]
	s_nop 0
	v_add_f32_e32 v96, v96, v97
	s_nop 1
	v_add_f32_dpp v96, v96, v96 quad_perm:[1,0,3,2] row_mask:0xf bank_mask:0xf
	s_nop 1
	v_add_f32_dpp v96, v96, v96 quad_perm:[2,3,0,1] row_mask:0xf bank_mask:0xf
	s_nop 1
	v_add_f32_dpp v96, v96, v96 row_half_mirror row_mask:0xf bank_mask:0xf
	s_nop 1
	v_add_f32_dpp v96, v96, v96 row_mirror row_mask:0xf bank_mask:0xf
	v_mov_b32_e32 v97, v96
	s_nop 1
	v_permlane16_swap_b32_e32 v97, v96
	v_add_f32_e32 v96, v96, v97
	v_mov_b32_e32 v97, v96
	s_nop 1
	v_permlane32_swap_b32_e32 v97, v96
	v_add_f32_e32 v96, v96, v97
	v_fmamk_f32 v96, v96, 0x3a000000, v130
	v_mul_f32_e32 v97, 0x4f800000, v96
	v_cmp_gt_f32_e32 vcc, s3, v96
	s_nop 1
	v_cndmask_b32_e32 v96, v96, v97, vcc
	v_sqrt_f32_e32 v97, v96
	s_nop 0
	v_add_u32_e32 v98, -1, v97
	v_add_u32_e32 v99, 1, v97
	v_fma_f32 v100, -v98, v97, v96
	v_fma_f32 v101, -v99, v97, v96
	v_cmp_ge_f32_e64 s[4:5], 0, v100
	s_nop 1
	v_cndmask_b32_e64 v97, v97, v98, s[4:5]
	v_cmp_lt_f32_e64 s[4:5], 0, v101
	s_nop 1
	v_cndmask_b32_e64 v97, v97, v99, s[4:5]
	v_mul_f32_e32 v98, 0x37800000, v97
	v_cndmask_b32_e32 v97, v97, v98, vcc
	v_cmp_class_f32_e32 vcc, v96, v131
	s_nop 1
	v_cndmask_b32_e32 v96, v97, v96, vcc
	v_div_scale_f32 v97, s[4:5], v96, v96, 1.0
	v_rcp_f32_e32 v98, v97
	v_div_scale_f32 v99, vcc, 1.0, v96, 1.0
	v_fma_f32 v100, -v97, v98, 1.0
	v_fmac_f32_e32 v98, v100, v98
	v_mul_f32_e32 v100, v99, v98
	v_fma_f32 v101, -v97, v100, v99
	v_fmac_f32_e32 v100, v101, v98
	v_fma_f32 v97, -v97, v100, v99
	v_div_fmas_f32 v97, v97, v98, v100
	v_div_fixup_f32 v142, v97, v96, 1.0
	v_pk_mul_f32 v[98:99], v[104:105], v[142:143] op_sel_hi:[1,0]
	v_pk_mul_f32 v[100:101], v[106:107], v[142:143] op_sel_hi:[1,0]
	v_pk_mul_f32 v[96:97], v[102:103], v[142:143] op_sel_hi:[1,0]
	v_pk_mul_f32 v[86:87], v[86:87], v[142:143] op_sel_hi:[1,0]
	v_pk_mul_f32 v[104:105], v[110:111], v[142:143] op_sel_hi:[1,0]
	v_pk_mul_f32 v[146:147], v[94:95], v[142:143] op_sel_hi:[1,0]
	v_pk_mul_f32 v[94:95], v[114:115], v[142:143] op_sel_hi:[1,0]
	v_pk_fma_f32 v[114:115], v[52:53], v[98:99], v[4:5]
	v_pk_fma_f32 v[110:111], v[56:57], v[100:101], v[8:9]
	v_pk_mul_f32 v[102:103], v[108:109], v[142:143] op_sel_hi:[1,0]
	v_pk_mul_f32 v[144:145], v[112:113], v[142:143] op_sel_hi:[1,0]
	v_pk_fma_f32 v[116:117], v[54:55], v[96:97], v[2:3]
	v_pk_fma_f32 v[112:113], v[58:59], v[86:87], v[6:7]
	v_pk_mul_f32 v[86:87], v[134:135], v[142:143] op_sel_hi:[1,0]
	v_max_f32_e64 v133, |v114|, |v115|
	v_max_f32_e64 v134, |v110|, |v111|
	v_pk_mul_f32 v[88:89], v[88:89], v[142:143] op_sel_hi:[1,0]
	v_pk_mul_f32 v[90:91], v[90:91], v[142:143] op_sel_hi:[1,0]
	v_pk_fma_f32 v[106:107], v[60:61], v[102:103], v[12:13]
	v_pk_fma_f32 v[102:103], v[64:65], v[104:105], v[16:17]
	v_max3_f32 v133, |v116|, |v117|, v133
	v_max3_f32 v134, |v112|, |v113|, v134
	v_pk_fma_f32 v[108:109], v[62:63], v[88:89], v[10:11]
	v_pk_fma_f32 v[104:105], v[66:67], v[90:91], v[14:15]
	v_max3_f32 v133, v133, s7, v134
	v_max_f32_e64 v134, |v106|, |v107|
	v_max_f32_e64 v135, |v102|, |v103|
	v_pk_mul_f32 v[92:93], v[92:93], v[142:143] op_sel_hi:[1,0]
	v_pk_fma_f32 v[98:99], v[68:69], v[144:145], v[20:21]
	v_pk_fma_f32 v[94:95], v[72:73], v[94:95], v[24:25]
	v_max3_f32 v134, |v108|, |v109|, v134
	v_max3_f32 v135, |v104|, |v105|, v135
	v_pk_fma_f32 v[100:101], v[70:71], v[92:93], v[18:19]
	v_pk_fma_f32 v[96:97], v[74:75], v[146:147], v[22:23]
	v_pk_mul_f32 v[88:89], v[136:137], v[142:143] op_sel_hi:[1,0]
	v_pk_fma_f32 v[92:93], v[78:79], v[86:87], v[26:27]
	v_pk_mul_f32 v[86:87], v[140:141], v[142:143] op_sel_hi:[1,0]
	v_max3_f32 v133, v133, v134, v135
	v_max_f32_e64 v134, |v98|, |v99|
	v_max_f32_e64 v135, |v94|, |v95|
	v_pk_fma_f32 v[90:91], v[76:77], v[88:89], v[28:29]
	v_pk_mul_f32 v[88:89], v[138:139], v[142:143] op_sel_hi:[1,0]
	v_pk_fma_f32 v[86:87], v[80:81], v[86:87], v[32:33]
	v_max3_f32 v134, |v100|, |v101|, v134
	v_max3_f32 v135, |v96|, |v97|, v135
	v_pk_fma_f32 v[88:89], v[82:83], v[88:89], v[30:31]
	v_max3_f32 v133, v133, v134, v135
	v_max_f32_e64 v134, |v90|, |v91|
	v_max_f32_e64 v135, |v86|, |v87|
	v_max3_f32 v134, |v92|, |v93|, v134
	v_max3_f32 v135, |v88|, |v89|, v135
	v_max3_f32 v133, v133, v134, v135
	s_nop 1
	v_max_f32_dpp v133, v133, v133 quad_perm:[1,0,3,2] row_mask:0xf bank_mask:0xf
	s_nop 1
	v_max_f32_dpp v133, v133, v133 quad_perm:[2,3,0,1] row_mask:0xf bank_mask:0xf
	s_nop 1
	v_max_f32_dpp v133, v133, v133 row_half_mirror row_mask:0xf bank_mask:0xf
	s_nop 1
	v_max_f32_dpp v133, v133, v133 row_mirror row_mask:0xf bank_mask:0xf
	v_mov_b32_e32 v134, v133
	s_nop 1
	v_permlane16_swap_b32_e32 v134, v133
	v_max_f32_e32 v133, v133, v134
	v_mov_b32_e32 v134, v133
	s_nop 1
	v_permlane32_swap_b32_e32 v134, v133
	v_max_f32_e32 v133, v133, v134
	s_and_saveexec_b64 s[4:5], s[0:1]
	s_cbranch_execz .LBB0_1121
	s_add_u32 s28, s22, s18
	s_addc_u32 s29, s23, s19
	v_mul_f32_e32 v134, 0x3c010204, v133
	global_store_dword v35, v134, s[28:29]
	s_branch .LBB0_1121

.LBB0_2014:
	global_load_dwordx2 v[92:93], v[56:57], off offset:-2048
	global_load_dwordx2 v[94:95], v[56:57], off offset:-1536
	global_load_dwordx2 v[96:97], v[56:57], off offset:-1024
	global_load_dwordx2 v[98:99], v[56:57], off offset:-512
	global_load_dwordx2 v[100:101], v[56:57], off
	global_load_dwordx2 v[102:103], v[56:57], off offset:512
	global_load_dwordx2 v[104:105], v[56:57], off offset:1024
	global_load_dwordx2 v[106:107], v[56:57], off offset:1536
	s_waitcnt vmcnt(7)
	v_cvt_f32_f16_sdwa v109, v92 dst_sel:DWORD dst_unused:UNUSED_PAD src0_sel:WORD_1
	v_cvt_f32_f16_sdwa v111, v93 dst_sel:DWORD dst_unused:UNUSED_PAD src0_sel:WORD_1
	v_cvt_f32_f16_e32 v110, v93
	s_waitcnt vmcnt(6)
	v_cvt_f32_f16_sdwa v93, v94 dst_sel:DWORD dst_unused:UNUSED_PAD src0_sel:WORD_1
	v_cvt_f32_f16_sdwa v113, v95 dst_sel:DWORD dst_unused:UNUSED_PAD src0_sel:WORD_1
	v_cvt_f32_f16_e32 v108, v92
	v_cvt_f32_f16_e32 v92, v94
	v_cvt_f32_f16_e32 v112, v95
	s_waitcnt vmcnt(5)
	v_cvt_f32_f16_sdwa v95, v96 dst_sel:DWORD dst_unused:UNUSED_PAD src0_sel:WORD_1
	v_cvt_f32_f16_sdwa v115, v97 dst_sel:DWORD dst_unused:UNUSED_PAD src0_sel:WORD_1
	v_cvt_f32_f16_e32 v94, v96
	v_cvt_f32_f16_e32 v114, v97
	s_waitcnt vmcnt(4)
	v_cvt_f32_f16_sdwa v97, v98 dst_sel:DWORD dst_unused:UNUSED_PAD src0_sel:WORD_1
	v_cvt_f32_f16_sdwa v117, v99 dst_sel:DWORD dst_unused:UNUSED_PAD src0_sel:WORD_1
	v_cvt_f32_f16_e32 v96, v98
	v_cvt_f32_f16_e32 v116, v99
	s_waitcnt vmcnt(3)
	v_cvt_f32_f16_sdwa v99, v100 dst_sel:DWORD dst_unused:UNUSED_PAD src0_sel:WORD_1
	v_cvt_f32_f16_e32 v98, v100
	v_cvt_f32_f16_sdwa v119, v101 dst_sel:DWORD dst_unused:UNUSED_PAD src0_sel:WORD_1
	v_cvt_f32_f16_e32 v118, v101
	s_waitcnt vmcnt(1)
	v_cvt_f32_f16_sdwa v141, v104 dst_sel:DWORD dst_unused:UNUSED_PAD src0_sel:WORD_1
	v_cvt_f32_f16_e32 v140, v104
	v_cvt_f32_f16_sdwa v143, v105 dst_sel:DWORD dst_unused:UNUSED_PAD src0_sel:WORD_1
	v_cvt_f32_f16_e32 v142, v105
	v_mov_b32_e32 v104, v109
	v_mov_b32_e32 v105, v93
	v_mov_b32_e32 v122, v111
	v_mov_b32_e32 v123, v113
	v_cvt_f32_f16_sdwa v101, v102 dst_sel:DWORD dst_unused:UNUSED_PAD src0_sel:WORD_1
	v_cvt_f32_f16_e32 v100, v102
	v_cvt_f32_f16_sdwa v121, v103 dst_sel:DWORD dst_unused:UNUSED_PAD src0_sel:WORD_1
	v_cvt_f32_f16_e32 v120, v103
	s_waitcnt vmcnt(0)
	v_cvt_f32_f16_sdwa v145, v106 dst_sel:DWORD dst_unused:UNUSED_PAD src0_sel:WORD_1
	v_cvt_f32_f16_e32 v144, v106
	v_cvt_f32_f16_sdwa v147, v107 dst_sel:DWORD dst_unused:UNUSED_PAD src0_sel:WORD_1
	v_cvt_f32_f16_e32 v146, v107
	v_mov_b32_e32 v102, v108
	v_mov_b32_e32 v103, v92
	v_mov_b32_e32 v106, v110
	v_mov_b32_e32 v107, v112
	v_mov_b32_e32 v150, v95
	v_mov_b32_e32 v151, v115
	v_pk_mul_f32 v[104:105], v[104:105], v[104:105]
	v_pk_mul_f32 v[122:123], v[122:123], v[122:123]
	v_mov_b32_e32 v148, v94
	v_mov_b32_e32 v149, v114
	v_pk_mul_f32 v[150:151], v[150:151], v[150:151]
	v_pk_fma_f32 v[102:103], v[102:103], v[102:103], v[104:105]
	v_pk_fma_f32 v[104:105], v[106:107], v[106:107], v[122:123]
	v_mul_f32_e32 v152, v97, v97
	v_mul_f32_e32 v154, v117, v117
	v_pk_fma_f32 v[106:107], v[148:149], v[148:149], v[150:151]
	v_pk_add_f32 v[102:103], v[102:103], v[104:105]
	v_pk_mul_f32 v[156:157], v[98:99], v[98:99]
	v_pk_mul_f32 v[158:159], v[118:119], v[118:119]
	v_pk_fma_f32 v[152:153], v[96:97], v[96:97], v[152:153] op_sel_hi:[1,1,0]
	v_pk_fma_f32 v[154:155], v[116:117], v[116:117], v[154:155] op_sel_hi:[1,1,0]
	v_pk_add_f32 v[104:105], v[106:107], v[106:107] op_sel:[0,1] op_sel_hi:[1,0]
	v_pk_add_f32 v[102:103], v[102:103], v[102:103] op_sel:[0,1] op_sel_hi:[1,0]
	v_mov_b32_e32 v162, v101
	v_mov_b32_e32 v163, v121
	v_mov_b32_e32 v153, v158
	v_mov_b32_e32 v155, v159
	v_mov_b32_e32 v105, v157
	v_mov_b32_e32 v103, v156
	v_mov_b32_e32 v160, v100
	v_mov_b32_e32 v161, v120
	v_pk_mul_f32 v[162:163], v[162:163], v[162:163]
	v_pk_add_f32 v[106:107], v[152:153], v[154:155]
	v_pk_add_f32 v[102:103], v[102:103], v[104:105]
	v_mul_f32_e32 v164, v141, v141
	v_mul_f32_e32 v166, v143, v143
	v_pk_fma_f32 v[122:123], v[160:161], v[160:161], v[162:163]
	v_pk_add_f32 v[102:103], v[102:103], v[106:107]
	v_pk_mul_f32 v[168:169], v[144:145], v[144:145]
	v_pk_mul_f32 v[170:171], v[146:147], v[146:147]
	v_pk_fma_f32 v[164:165], v[140:141], v[140:141], v[164:165] op_sel_hi:[1,1,0]
	v_pk_fma_f32 v[166:167], v[142:143], v[142:143], v[166:167] op_sel_hi:[1,1,0]
	v_pk_add_f32 v[122:123], v[122:123], v[122:123] op_sel:[0,1] op_sel_hi:[1,0]
	v_pk_add_f32 v[102:103], v[102:103], v[102:103] op_sel:[0,1] op_sel_hi:[1,0]
	v_mov_b32_e32 v165, v170
	v_mov_b32_e32 v167, v171
	v_mov_b32_e32 v123, v169
	v_mov_b32_e32 v103, v168
	v_pk_add_f32 v[148:149], v[164:165], v[166:167]
	v_pk_add_f32 v[102:103], v[102:103], v[122:123]
	s_nop 0
	v_pk_add_f32 v[102:103], v[102:103], v[148:149]
	s_nop 0
	v_add_f32_e32 v102, v102, v103
	s_nop 1
	v_add_f32_dpp v102, v102, v102 quad_perm:[1,0,3,2] row_mask:0xf bank_mask:0xf
	s_nop 1
	v_add_f32_dpp v102, v102, v102 quad_perm:[2,3,0,1] row_mask:0xf bank_mask:0xf
	s_nop 1
	v_add_f32_dpp v102, v102, v102 row_half_mirror row_mask:0xf bank_mask:0xf
	s_nop 1
	v_add_f32_dpp v102, v102, v102 row_mirror row_mask:0xf bank_mask:0xf
	v_mov_b32_e32 v103, v102
	s_nop 1
	v_permlane16_swap_b32_e32 v103, v102
	v_add_f32_e32 v102, v102, v103
	v_mov_b32_e32 v103, v102
	s_nop 1
	v_permlane32_swap_b32_e32 v103, v102
	v_add_f32_e32 v102, v102, v103
	v_fmamk_f32 v102, v102, 0x3a000000, v136
	v_mul_f32_e32 v103, 0x4f800000, v102
	v_cmp_gt_f32_e32 vcc, s3, v102
	s_nop 1
	v_cndmask_b32_e32 v102, v102, v103, vcc
	v_sqrt_f32_e32 v103, v102
	s_nop 0
	v_add_u32_e32 v104, -1, v103
	v_add_u32_e32 v105, 1, v103
	v_fma_f32 v106, -v104, v103, v102
	v_fma_f32 v107, -v105, v103, v102
	v_cmp_ge_f32_e64 s[4:5], 0, v106
	s_nop 1
	v_cndmask_b32_e64 v103, v103, v104, s[4:5]
	v_cmp_lt_f32_e64 s[4:5], 0, v107
	s_nop 1
	v_cndmask_b32_e64 v103, v103, v105, s[4:5]
	v_mul_f32_e32 v104, 0x37800000, v103
	v_cndmask_b32_e32 v103, v103, v104, vcc
	v_cmp_class_f32_e32 vcc, v102, v137
	s_nop 1
	v_cndmask_b32_e32 v102, v103, v102, vcc
	v_div_scale_f32 v103, s[4:5], v102, v102, 1.0
	v_rcp_f32_e32 v104, v103
	v_div_scale_f32 v105, vcc, 1.0, v102, 1.0
	v_fma_f32 v106, -v103, v104, 1.0
	v_fmac_f32_e32 v104, v106, v104
	v_mul_f32_e32 v106, v105, v104
	v_fma_f32 v107, -v103, v106, v105
	v_fmac_f32_e32 v106, v107, v104
	v_fma_f32 v103, -v103, v106, v105
	v_div_fmas_f32 v103, v103, v104, v106
	v_div_fixup_f32 v148, v103, v102, 1.0
	v_pk_mul_f32 v[104:105], v[110:111], v[148:149] op_sel_hi:[1,0]
	v_pk_mul_f32 v[106:107], v[112:113], v[148:149] op_sel_hi:[1,0]
	v_pk_mul_f32 v[102:103], v[108:109], v[148:149] op_sel_hi:[1,0]
	v_pk_mul_f32 v[92:93], v[92:93], v[148:149] op_sel_hi:[1,0]
	v_pk_mul_f32 v[110:111], v[116:117], v[148:149] op_sel_hi:[1,0]
	v_pk_mul_f32 v[152:153], v[100:101], v[148:149] op_sel_hi:[1,0]
	v_pk_mul_f32 v[100:101], v[120:121], v[148:149] op_sel_hi:[1,0]
	v_pk_fma_f32 v[120:121], v[58:59], v[104:105], v[4:5]
	v_pk_fma_f32 v[116:117], v[62:63], v[106:107], v[8:9]
	v_pk_mul_f32 v[108:109], v[114:115], v[148:149] op_sel_hi:[1,0]
	v_pk_mul_f32 v[150:151], v[118:119], v[148:149] op_sel_hi:[1,0]
	v_pk_fma_f32 v[122:123], v[60:61], v[102:103], v[2:3]
	v_pk_fma_f32 v[118:119], v[64:65], v[92:93], v[6:7]
	v_pk_mul_f32 v[92:93], v[140:141], v[148:149] op_sel_hi:[1,0]
	v_max_f32_e64 v139, |v120|, |v121|
	v_max_f32_e64 v140, |v116|, |v117|
	v_pk_mul_f32 v[94:95], v[94:95], v[148:149] op_sel_hi:[1,0]
	v_pk_mul_f32 v[96:97], v[96:97], v[148:149] op_sel_hi:[1,0]
	v_pk_fma_f32 v[112:113], v[66:67], v[108:109], v[12:13]
	v_pk_fma_f32 v[108:109], v[70:71], v[110:111], v[16:17]
	v_max3_f32 v139, |v122|, |v123|, v139
	v_max3_f32 v140, |v118|, |v119|, v140
	v_pk_fma_f32 v[114:115], v[68:69], v[94:95], v[10:11]
	v_pk_fma_f32 v[110:111], v[72:73], v[96:97], v[14:15]
	v_max3_f32 v139, v139, s7, v140
	v_max_f32_e64 v140, |v112|, |v113|
	v_max_f32_e64 v141, |v108|, |v109|
	v_pk_mul_f32 v[98:99], v[98:99], v[148:149] op_sel_hi:[1,0]
	v_pk_fma_f32 v[104:105], v[74:75], v[150:151], v[20:21]
	v_pk_fma_f32 v[100:101], v[78:79], v[100:101], v[24:25]
	v_max3_f32 v140, |v114|, |v115|, v140
	v_max3_f32 v141, |v110|, |v111|, v141
	v_pk_fma_f32 v[106:107], v[76:77], v[98:99], v[18:19]
	v_pk_fma_f32 v[102:103], v[80:81], v[152:153], v[22:23]
	v_pk_mul_f32 v[94:95], v[142:143], v[148:149] op_sel_hi:[1,0]
	v_pk_fma_f32 v[98:99], v[84:85], v[92:93], v[26:27]
	v_pk_mul_f32 v[92:93], v[146:147], v[148:149] op_sel_hi:[1,0]
	v_max3_f32 v139, v139, v140, v141
	v_max_f32_e64 v140, |v104|, |v105|
	v_max_f32_e64 v141, |v100|, |v101|
	v_pk_fma_f32 v[96:97], v[82:83], v[94:95], v[28:29]
	v_pk_mul_f32 v[94:95], v[144:145], v[148:149] op_sel_hi:[1,0]
	v_pk_fma_f32 v[92:93], v[86:87], v[92:93], v[32:33]
	v_max3_f32 v140, |v106|, |v107|, v140
	v_max3_f32 v141, |v102|, |v103|, v141
	v_pk_fma_f32 v[94:95], v[88:89], v[94:95], v[30:31]
	v_max3_f32 v139, v139, v140, v141
	v_max_f32_e64 v140, |v96|, |v97|
	v_max_f32_e64 v141, |v92|, |v93|
	v_max3_f32 v140, |v98|, |v99|, v140
	v_max3_f32 v141, |v94|, |v95|, v141
	v_max3_f32 v139, v139, v140, v141
	s_nop 1
	v_max_f32_dpp v139, v139, v139 quad_perm:[1,0,3,2] row_mask:0xf bank_mask:0xf
	s_nop 1
	v_max_f32_dpp v139, v139, v139 quad_perm:[2,3,0,1] row_mask:0xf bank_mask:0xf
	s_nop 1
	v_max_f32_dpp v139, v139, v139 row_half_mirror row_mask:0xf bank_mask:0xf
	s_nop 1
	v_max_f32_dpp v139, v139, v139 row_mirror row_mask:0xf bank_mask:0xf
	v_mov_b32_e32 v140, v139
	s_nop 1
	v_permlane16_swap_b32_e32 v140, v139
	v_max_f32_e32 v139, v139, v140
	v_mov_b32_e32 v140, v139
	s_nop 1
	v_permlane32_swap_b32_e32 v140, v139
	v_max_f32_e32 v139, v139, v140
	s_and_saveexec_b64 s[4:5], s[0:1]
	s_cbranch_execz .LBB0_2013
	s_add_u32 s26, s20, s18
	s_addc_u32 s27, s21, s19
	v_mul_f32_e32 v140, 0x3c010204, v139
	global_store_dword v35, v140, s[26:27]
	s_branch .LBB0_2013

.LBB0_3611:
	s_waitcnt lgkmcnt(2)
	v_lshl_add_u64 v[94:95], s[96:97], 0, v[58:59]
	v_add_co_u32_e32 v94, vcc, 0x32a00000, v94
	s_nop 1
	v_addc_co_u32_e32 v95, vcc, 0, v95, vcc
	s_waitcnt lgkmcnt(1)
	global_load_dwordx2 v[96:97], v[94:95], off
	s_waitcnt lgkmcnt(0)
	global_load_dwordx2 v[98:99], v[94:95], off offset:512
	global_load_dwordx2 v[100:101], v[94:95], off offset:1024
	global_load_dwordx2 v[102:103], v[94:95], off offset:1536
	global_load_dwordx2 v[104:105], v[94:95], off offset:2048
	global_load_dwordx2 v[106:107], v[94:95], off offset:2560
	global_load_dwordx2 v[108:109], v[94:95], off offset:3072
	s_nop 0
	global_load_dwordx2 v[94:95], v[94:95], off offset:3584
	s_waitcnt vmcnt(7)
	v_cvt_f32_f16_e32 v110, v96
	v_cvt_f32_f16_sdwa v111, v96 dst_sel:DWORD dst_unused:UNUSED_PAD src0_sel:WORD_1
	v_cvt_f32_f16_e32 v96, v97
	v_cvt_f32_f16_sdwa v97, v97 dst_sel:DWORD dst_unused:UNUSED_PAD src0_sel:WORD_1
	s_waitcnt vmcnt(6)
	v_cvt_f32_f16_e32 v112, v98
	v_cvt_f32_f16_sdwa v113, v98 dst_sel:DWORD dst_unused:UNUSED_PAD src0_sel:WORD_1
	v_cvt_f32_f16_e32 v98, v99
	v_cvt_f32_f16_sdwa v99, v99 dst_sel:DWORD dst_unused:UNUSED_PAD src0_sel:WORD_1
	s_waitcnt vmcnt(5)
	v_cvt_f32_f16_e32 v114, v100
	v_cvt_f32_f16_sdwa v115, v100 dst_sel:DWORD dst_unused:UNUSED_PAD src0_sel:WORD_1
	v_cvt_f32_f16_e32 v100, v101
	v_cvt_f32_f16_sdwa v101, v101 dst_sel:DWORD dst_unused:UNUSED_PAD src0_sel:WORD_1
	s_waitcnt vmcnt(4)
	v_cvt_f32_f16_e32 v116, v102
	v_cvt_f32_f16_sdwa v117, v102 dst_sel:DWORD dst_unused:UNUSED_PAD src0_sel:WORD_1
	v_cvt_f32_f16_e32 v102, v103
	v_cvt_f32_f16_sdwa v103, v103 dst_sel:DWORD dst_unused:UNUSED_PAD src0_sel:WORD_1
	s_waitcnt vmcnt(3)
	v_cvt_f32_f16_e32 v118, v104
	v_cvt_f32_f16_sdwa v119, v104 dst_sel:DWORD dst_unused:UNUSED_PAD src0_sel:WORD_1
	v_cvt_f32_f16_e32 v104, v105
	v_cvt_f32_f16_sdwa v105, v105 dst_sel:DWORD dst_unused:UNUSED_PAD src0_sel:WORD_1
	s_waitcnt vmcnt(1)
	v_cvt_f32_f16_e32 v130, v108
	v_cvt_f32_f16_sdwa v131, v108 dst_sel:DWORD dst_unused:UNUSED_PAD src0_sel:WORD_1
	v_cvt_f32_f16_e32 v148, v109
	v_cvt_f32_f16_sdwa v149, v109 dst_sel:DWORD dst_unused:UNUSED_PAD src0_sel:WORD_1
	v_mov_b32_e32 v108, v111
	v_mov_b32_e32 v109, v113
	v_mov_b32_e32 v122, v97
	v_mov_b32_e32 v123, v99
	v_cvt_f32_f16_e32 v126, v106
	v_cvt_f32_f16_sdwa v127, v106 dst_sel:DWORD dst_unused:UNUSED_PAD src0_sel:WORD_1
	v_cvt_f32_f16_e32 v128, v107
	v_cvt_f32_f16_sdwa v129, v107 dst_sel:DWORD dst_unused:UNUSED_PAD src0_sel:WORD_1
	v_mov_b32_e32 v106, v110
	v_mov_b32_e32 v107, v112
	v_mov_b32_e32 v120, v96
	v_mov_b32_e32 v121, v98
	v_mov_b32_e32 v152, v115
	v_mov_b32_e32 v153, v101
	v_pk_mul_f32 v[108:109], v[108:109], v[108:109]
	v_pk_mul_f32 v[122:123], v[122:123], v[122:123]
	v_mov_b32_e32 v124, v114
	v_mov_b32_e32 v125, v100
	v_pk_mul_f32 v[152:153], v[152:153], v[152:153]
	v_pk_fma_f32 v[106:107], v[106:107], v[106:107], v[108:109]
	v_pk_fma_f32 v[108:109], v[120:121], v[120:121], v[122:123]
	v_mul_f32_e32 v154, v117, v117
	v_mul_f32_e32 v156, v103, v103
	v_pk_fma_f32 v[120:121], v[124:125], v[124:125], v[152:153]
	v_pk_add_f32 v[106:107], v[106:107], v[108:109]
	s_waitcnt vmcnt(0)
	v_cvt_f32_f16_e32 v150, v94
	v_cvt_f32_f16_sdwa v151, v94 dst_sel:DWORD dst_unused:UNUSED_PAD src0_sel:WORD_1
	v_cvt_f32_f16_e32 v94, v95
	v_cvt_f32_f16_sdwa v95, v95 dst_sel:DWORD dst_unused:UNUSED_PAD src0_sel:WORD_1
	v_pk_mul_f32 v[158:159], v[118:119], v[118:119]
	v_pk_mul_f32 v[160:161], v[104:105], v[104:105]
	v_pk_fma_f32 v[154:155], v[116:117], v[116:117], v[154:155] op_sel_hi:[1,1,0]
	v_pk_fma_f32 v[156:157], v[102:103], v[102:103], v[156:157] op_sel_hi:[1,1,0]
	v_pk_add_f32 v[108:109], v[120:121], v[120:121] op_sel:[0,1] op_sel_hi:[1,0]
	v_pk_add_f32 v[106:107], v[106:107], v[106:107] op_sel:[0,1] op_sel_hi:[1,0]
	v_mov_b32_e32 v164, v127
	v_mov_b32_e32 v165, v129
	v_mov_b32_e32 v155, v160
	v_mov_b32_e32 v157, v161
	v_mov_b32_e32 v109, v159
	v_mov_b32_e32 v107, v158
	v_mov_b32_e32 v162, v126
	v_mov_b32_e32 v163, v128
	v_pk_mul_f32 v[164:165], v[164:165], v[164:165]
	v_pk_add_f32 v[120:121], v[154:155], v[156:157]
	v_pk_add_f32 v[106:107], v[106:107], v[108:109]
	v_mul_f32_e32 v166, v131, v131
	v_mul_f32_e32 v168, v149, v149
	v_pk_fma_f32 v[122:123], v[162:163], v[162:163], v[164:165]
	v_pk_add_f32 v[106:107], v[106:107], v[120:121]
	v_pk_mul_f32 v[170:171], v[150:151], v[150:151]
	v_pk_mul_f32 v[172:173], v[94:95], v[94:95]
	v_pk_fma_f32 v[166:167], v[130:131], v[130:131], v[166:167] op_sel_hi:[1,1,0]
	v_pk_fma_f32 v[168:169], v[148:149], v[148:149], v[168:169] op_sel_hi:[1,1,0]
	v_pk_add_f32 v[122:123], v[122:123], v[122:123] op_sel:[0,1] op_sel_hi:[1,0]
	v_pk_add_f32 v[106:107], v[106:107], v[106:107] op_sel:[0,1] op_sel_hi:[1,0]
	v_mov_b32_e32 v167, v172
	v_mov_b32_e32 v123, v171
	v_mov_b32_e32 v107, v170
	v_mov_b32_e32 v169, v173
	v_pk_add_f32 v[106:107], v[106:107], v[122:123]
	v_pk_add_f32 v[108:109], v[166:167], v[168:169]
	s_nop 0
	v_pk_add_f32 v[106:107], v[106:107], v[108:109]
	s_nop 0
	v_add_f32_e32 v106, v106, v107
	s_nop 1
	v_add_f32_dpp v106, v106, v106 quad_perm:[1,0,3,2] row_mask:0xf bank_mask:0xf
	s_nop 1
	v_add_f32_dpp v106, v106, v106 quad_perm:[2,3,0,1] row_mask:0xf bank_mask:0xf
	s_nop 1
	v_add_f32_dpp v106, v106, v106 row_half_mirror row_mask:0xf bank_mask:0xf
	s_nop 1
	v_add_f32_dpp v106, v106, v106 row_mirror row_mask:0xf bank_mask:0xf
	v_mov_b32_e32 v107, v106
	s_nop 1
	v_permlane16_swap_b32_e32 v107, v106
	v_add_f32_e32 v106, v106, v107
	v_mov_b32_e32 v107, v106
	s_nop 1
	v_permlane32_swap_b32_e32 v107, v106
	v_add_f32_e32 v106, v106, v107
	v_fmamk_f32 v106, v106, 0x3a000000, v144
	v_mul_f32_e32 v107, 0x4f800000, v106
	v_cmp_gt_f32_e32 vcc, s57, v106
	s_nop 1
	v_cndmask_b32_e32 v106, v106, v107, vcc
	v_sqrt_f32_e32 v107, v106
	s_nop 0
	v_add_u32_e32 v108, -1, v107
	v_add_u32_e32 v109, 1, v107
	v_fma_f32 v120, -v108, v107, v106
	v_fma_f32 v121, -v109, v107, v106
	v_cmp_ge_f32_e64 s[4:5], 0, v120
	s_nop 1
	v_cndmask_b32_e64 v107, v107, v108, s[4:5]
	v_cmp_lt_f32_e64 s[4:5], 0, v121
	s_nop 1
	v_cndmask_b32_e64 v107, v107, v109, s[4:5]
	v_mul_f32_e32 v108, 0x37800000, v107
	v_cndmask_b32_e32 v107, v107, v108, vcc
	v_cmp_class_f32_e32 vcc, v106, v145
	s_nop 1
	v_cndmask_b32_e32 v106, v107, v106, vcc
	v_div_scale_f32 v107, s[4:5], v106, v106, 1.0
	v_rcp_f32_e32 v108, v107
	v_div_scale_f32 v109, vcc, 1.0, v106, 1.0
	v_fma_f32 v120, -v107, v108, 1.0
	v_fmac_f32_e32 v108, v120, v108
	v_mul_f32_e32 v120, v109, v108
	v_fma_f32 v121, -v107, v120, v109
	v_fmac_f32_e32 v120, v121, v108
	v_fma_f32 v107, -v107, v120, v109
	v_div_fmas_f32 v107, v107, v108, v120
	v_div_fixup_f32 v152, v107, v106, 1.0
	v_pk_mul_f32 v[96:97], v[96:97], v[152:153] op_sel_hi:[1,0]
	v_pk_mul_f32 v[98:99], v[98:99], v[152:153] op_sel_hi:[1,0]
	v_pk_mul_f32 v[106:107], v[110:111], v[152:153] op_sel_hi:[1,0]
	v_pk_mul_f32 v[108:109], v[112:113], v[152:153] op_sel_hi:[1,0]
	v_pk_mul_f32 v[154:155], v[118:119], v[152:153] op_sel_hi:[1,0]
	v_pk_fma_f32 v[122:123], v[62:63], v[96:97], v[4:5]
	v_pk_fma_f32 v[118:119], v[66:67], v[98:99], v[8:9]
	v_pk_mul_f32 v[110:111], v[114:115], v[152:153] op_sel_hi:[1,0]
	v_pk_mul_f32 v[100:101], v[100:101], v[152:153] op_sel_hi:[1,0]
	v_pk_mul_f32 v[102:103], v[102:103], v[152:153] op_sel_hi:[1,0]
	v_pk_fma_f32 v[124:125], v[64:65], v[106:107], v[2:3]
	v_pk_fma_f32 v[120:121], v[68:69], v[108:109], v[6:7]
	v_pk_mul_f32 v[96:97], v[126:127], v[152:153] op_sel_hi:[1,0]
	v_max_f32_e64 v126, |v122|, |v123|
	v_max_f32_e64 v127, |v118|, |v119|
	v_pk_mul_f32 v[112:113], v[116:117], v[152:153] op_sel_hi:[1,0]
	v_pk_fma_f32 v[114:115], v[70:71], v[100:101], v[12:13]
	v_pk_fma_f32 v[116:117], v[72:73], v[110:111], v[10:11]
	v_pk_fma_f32 v[110:111], v[74:75], v[102:103], v[16:17]
	v_max3_f32 v126, |v124|, |v125|, v126
	v_max3_f32 v127, |v120|, |v121|, v127
	v_pk_mul_f32 v[104:105], v[104:105], v[152:153] op_sel_hi:[1,0]
	v_pk_fma_f32 v[112:113], v[76:77], v[112:113], v[14:15]
	v_pk_mul_f32 v[98:99], v[128:129], v[152:153] op_sel_hi:[1,0]
	v_max3_f32 v126, v126, s58, v127
	v_max_f32_e64 v127, |v114|, |v115|
	v_max_f32_e64 v128, |v110|, |v111|
	v_pk_fma_f32 v[104:105], v[78:79], v[104:105], v[20:21]
	v_pk_fma_f32 v[102:103], v[82:83], v[98:99], v[24:25]
	v_max3_f32 v127, |v116|, |v117|, v127
	v_max3_f32 v128, |v112|, |v113|, v128
	v_pk_fma_f32 v[106:107], v[80:81], v[154:155], v[18:19]
	v_pk_fma_f32 v[108:109], v[84:85], v[96:97], v[22:23]
	v_pk_mul_f32 v[96:97], v[148:149], v[152:153] op_sel_hi:[1,0]
	v_pk_mul_f32 v[94:95], v[94:95], v[152:153] op_sel_hi:[1,0]
	v_max3_f32 v126, v126, v127, v128
	v_max_f32_e64 v127, |v104|, |v105|
	v_max_f32_e64 v128, |v102|, |v103|
	v_pk_mul_f32 v[98:99], v[130:131], v[152:153] op_sel_hi:[1,0]
	v_pk_fma_f32 v[96:97], v[86:87], v[96:97], v[28:29]
	v_pk_mul_f32 v[100:101], v[150:151], v[152:153] op_sel_hi:[1,0]
	v_pk_fma_f32 v[94:95], v[90:91], v[94:95], v[32:33]
	v_max3_f32 v127, |v106|, |v107|, v127
	v_max3_f32 v128, |v108|, |v109|, v128
	v_pk_fma_f32 v[98:99], v[88:89], v[98:99], v[26:27]
	v_pk_fma_f32 v[100:101], v[92:93], v[100:101], v[30:31]
	v_max3_f32 v126, v126, v127, v128
	v_max_f32_e64 v127, |v96|, |v97|
	v_max_f32_e64 v128, |v94|, |v95|
	v_max3_f32 v127, |v98|, |v99|, v127
	v_max3_f32 v128, |v100|, |v101|, v128
	v_max3_f32 v126, v126, v127, v128
	s_nop 1
	v_max_f32_dpp v126, v126, v126 quad_perm:[1,0,3,2] row_mask:0xf bank_mask:0xf
	s_nop 1
	v_max_f32_dpp v126, v126, v126 quad_perm:[2,3,0,1] row_mask:0xf bank_mask:0xf
	s_nop 1
	v_max_f32_dpp v126, v126, v126 row_half_mirror row_mask:0xf bank_mask:0xf
	s_nop 1
	v_max_f32_dpp v126, v126, v126 row_mirror row_mask:0xf bank_mask:0xf
	v_mov_b32_e32 v127, v126
	s_nop 1
	v_permlane16_swap_b32_e32 v127, v126
	v_max_f32_e32 v126, v126, v127
	v_mov_b32_e32 v127, v126
	s_nop 1
	v_permlane32_swap_b32_e32 v127, v126
	v_max_f32_e32 v126, v126, v127
	s_and_saveexec_b64 s[4:5], s[0:1]
	s_cbranch_execz .LBB0_3613
	s_add_u32 s6, s96, s22
	s_addc_u32 s7, s97, s23
	v_mul_f32_e32 v127, 0x3c010204, v126
	global_store_dword v37, v127, s[6:7]
